# v49 + per-segment counts copied during the scan phase and tail lane-index registers set up early (nothing left between gather end and first post-gather barrier)
# baseline (speedup 1.0000x reference)
_Z7vq_mainPKfPKiS0_PfPhPdPi:
	s_load_dwordx4 s[4:7], s[0:1], 0x0
	s_load_dwordx2 s[22:23], s[0:1], 0x10
	s_load_dwordx2 s[20:21], s[0:1], 0x18
	s_load_dwordx4 s[12:15], s[0:1], 0x20
	s_load_dwordx2 s[10:11], s[0:1], 0x30
	s_and_b32 s3, s2, 7
	s_lshl_b32 s3, s3, 6
	s_lshr_b32 s16, s2, 3
	s_add_i32 s16, s16, s3
	s_lshr_b32 s18, s16, 5
	s_mov_b32 s19, 0
	s_and_b32 s28, s16, 31
	s_lshl_b32 s28, s28, 4
	s_add_i32 s29, s28, 1
	v_readfirstlane_b32 s17, v0
	v_and_b32_e32 v1, 63, v0
	v_lshlrev_b32_e32 v66, 4, v0
	s_lshr_b32 s17, s17, 6
	s_lshl_b32 s24, s17, 4
	s_lshl_b32 s30, s18, 15
	s_lshl_b32 s31, s18, 23
	v_add_u32_e32 v67, 0x1000, v66
	v_add_u32_e32 v68, 0x2000, v66
	v_add_u32_e32 v69, 0x3000, v66
	v_add_u32_e32 v70, 0x4000, v66
	v_add_u32_e32 v71, 0x5000, v66
	v_add_u32_e32 v72, 0x6000, v66
	v_add_u32_e32 v73, 0x7000, v66
	s_movk_i32 s9, 0x810
	s_mov_b32 s3, 0x8100
	s_mul_i32 s36, s29, 0x810
	v_mov_b32_e32 v141, s36
	v_sub_u32_e32 v141, 0, v141
	s_waitcnt lgkmcnt(0)
	s_add_u32 s34, s6, s30
	s_addc_u32 s35, s7, 0
	s_add_u32 s32, s4, s31
	s_addc_u32 s33, s5, 0
	global_load_dwordx4 v[74:77], v66, s[34:35]
	global_load_dwordx4 v[78:81], v67, s[34:35]
	global_load_dwordx4 v[82:85], v68, s[34:35]
	global_load_dwordx4 v[86:89], v69, s[34:35]
	global_load_dwordx4 v[90:93], v70, s[34:35]
	global_load_dwordx4 v[94:97], v71, s[34:35]
	global_load_dwordx4 v[98:101], v72, s[34:35]
	global_load_dwordx4 v[102:105], v73, s[34:35]
	v_and_b32_e32 v150, 15, v0
	v_or_b32_e32 v150, s24, v150
	v_and_b32_e32 v151, 48, v0
	v_lshl_or_b32 v150, v150, 10, v151
	global_load_dwordx4 v[62:65], v150, s[22:23] offset:0
	global_load_dwordx4 v[58:61], v150, s[22:23] offset:64
	global_load_dwordx4 v[54:57], v150, s[22:23] offset:128
	global_load_dwordx4 v[50:53], v150, s[22:23] offset:192
	global_load_dwordx4 v[46:49], v150, s[22:23] offset:256
	global_load_dwordx4 v[42:45], v150, s[22:23] offset:320
	global_load_dwordx4 v[38:41], v150, s[22:23] offset:384
	global_load_dwordx4 v[34:37], v150, s[22:23] offset:448
	global_load_dwordx4 v[30:33], v150, s[22:23] offset:512
	global_load_dwordx4 v[26:29], v150, s[22:23] offset:576
	global_load_dwordx4 v[22:25], v150, s[22:23] offset:640
	global_load_dwordx4 v[18:21], v150, s[22:23] offset:704
	global_load_dwordx4 v[14:17], v150, s[22:23] offset:768
	global_load_dwordx4 v[10:13], v150, s[22:23] offset:832
	global_load_dwordx4 v[6:9], v150, s[22:23] offset:896
	global_load_dwordx4 v[2:5], v150, s[22:23] offset:960
	v_and_b32_e32 v138, 15, v0
	v_lshlrev_b32_e32 v139, 2, v1
	v_bfe_u32 v140, v0, 4, 2
	v_mov_b32_e32 v142, 1
	v_mov_b32_e32 v143, 4
	v_mov_b32_e32 v144, 0x11100
	v_lshlrev_b32_e32 v145, 8, v0
	v_lshlrev_b32_e32 v148, 3, v0
	v_mov_b32_e32 v152, 0
	v_mov_b32_e32 v153, 0
	ds_write_b64 v148, v[152:153] offset:32768
	ds_write_b64 v148, v[152:153] offset:34832
	ds_write_b64 v148, v[152:153] offset:36896
	ds_write_b64 v148, v[152:153] offset:38960
	ds_write_b64 v148, v[152:153] offset:41024
	ds_write_b64 v148, v[152:153] offset:43088
	ds_write_b64 v148, v[152:153] offset:45152
	ds_write_b64 v148, v[152:153] offset:47216
	ds_write_b64 v148, v[152:153] offset:49280
	ds_write_b64 v148, v[152:153] offset:51344
	ds_write_b64 v148, v[152:153] offset:53408
	ds_write_b64 v148, v[152:153] offset:55472
	ds_write_b64 v148, v[152:153] offset:57536
	ds_write_b64 v148, v[152:153] offset:59600
	ds_write_b64 v148, v[152:153] offset:61664
	ds_write_b64 v148, v[152:153] offset:63728
	v_cmp_gt_u32_e32 vcc, 16, v0
	s_and_saveexec_b64 s[30:31], vcc
	v_mul_u32_u24_e32 v151, 0x810, v0
	ds_write_b64 v151, v[152:153] offset:34816
	v_mov_b32_e32 v150, 0x11540
	v_mov_b32_e32 v149, 8
	ds_write_b32 v150, v149
	s_mov_b64 exec, s[30:31]
	s_waitcnt lgkmcnt(0)
	s_barrier
	s_waitcnt vmcnt(16)
	v_mad_u32_u24 v74, v74, s9, v141
	v_mad_u32_u24 v75, v75, s9, v141
	v_mad_u32_u24 v76, v76, s9, v141
	v_mad_u32_u24 v77, v77, s9, v141
	v_mad_u32_u24 v78, v78, s9, v141
	v_mad_u32_u24 v79, v79, s9, v141
	v_mad_u32_u24 v80, v80, s9, v141
	v_mad_u32_u24 v81, v81, s9, v141
	v_mad_u32_u24 v82, v82, s9, v141
	v_mad_u32_u24 v83, v83, s9, v141
	v_mad_u32_u24 v84, v84, s9, v141
	v_mad_u32_u24 v85, v85, s9, v141
	v_mad_u32_u24 v86, v86, s9, v141
	v_mad_u32_u24 v87, v87, s9, v141
	v_mad_u32_u24 v88, v88, s9, v141
	v_mad_u32_u24 v89, v89, s9, v141
	v_mad_u32_u24 v90, v90, s9, v141
	v_mad_u32_u24 v91, v91, s9, v141
	v_mad_u32_u24 v92, v92, s9, v141
	v_mad_u32_u24 v93, v93, s9, v141
	v_mad_u32_u24 v94, v94, s9, v141
	v_mad_u32_u24 v95, v95, s9, v141
	v_mad_u32_u24 v96, v96, s9, v141
	v_mad_u32_u24 v97, v97, s9, v141
	v_mad_u32_u24 v98, v98, s9, v141
	v_mad_u32_u24 v99, v99, s9, v141
	v_mad_u32_u24 v100, v100, s9, v141
	v_mad_u32_u24 v101, v101, s9, v141
	v_mad_u32_u24 v102, v102, s9, v141
	v_mad_u32_u24 v103, v103, s9, v141
	v_mad_u32_u24 v104, v104, s9, v141
	v_mad_u32_u24 v105, v105, s9, v141
	v_cmp_gt_u32_e64 s[36:37], s3, v74
	v_cmp_gt_u32_e64 s[38:39], s3, v75
	v_cmp_gt_u32_e64 s[40:41], s3, v76
	v_cmp_gt_u32_e64 s[42:43], s3, v77
	v_cmp_gt_u32_e64 s[44:45], s3, v78
	v_cmp_gt_u32_e64 s[46:47], s3, v79
	v_cmp_gt_u32_e64 s[48:49], s3, v80
	v_cmp_gt_u32_e64 s[50:51], s3, v81
	v_cmp_gt_u32_e64 s[52:53], s3, v82
	v_cmp_gt_u32_e64 s[54:55], s3, v83
	v_cmp_gt_u32_e64 s[56:57], s3, v84
	v_cmp_gt_u32_e64 s[58:59], s3, v85
	v_cmp_gt_u32_e64 s[60:61], s3, v86
	v_cmp_gt_u32_e64 s[62:63], s3, v87
	v_cmp_gt_u32_e64 s[64:65], s3, v88
	v_cmp_gt_u32_e64 s[66:67], s3, v89
	v_cmp_gt_u32_e64 s[68:69], s3, v90
	v_cmp_gt_u32_e64 s[70:71], s3, v91
	v_cmp_gt_u32_e64 s[72:73], s3, v92
	v_cmp_gt_u32_e64 s[74:75], s3, v93
	v_cmp_gt_u32_e64 s[76:77], s3, v94
	v_cmp_gt_u32_e64 s[78:79], s3, v95
	v_cmp_gt_u32_e64 s[80:81], s3, v96
	v_cmp_gt_u32_e64 s[82:83], s3, v97
	v_cmp_gt_u32_e64 s[84:85], s3, v98
	v_cmp_gt_u32_e64 s[86:87], s3, v99
	v_cmp_gt_u32_e64 s[88:89], s3, v100
	v_cmp_gt_u32_e64 s[90:91], s3, v101
	v_cmp_gt_u32_e64 s[92:93], s3, v102
	v_cmp_gt_u32_e64 s[94:95], s3, v103
	v_cmp_gt_u32_e64 s[96:97], s3, v104
	v_cmp_gt_u32_e64 s[98:99], s3, v105
	s_mov_b64 exec, s[36:37]
	ds_add_u32 v74, v142 offset:34816
	s_mov_b64 exec, s[38:39]
	ds_add_u32 v75, v142 offset:34816
	s_mov_b64 exec, s[40:41]
	ds_add_u32 v76, v142 offset:34816
	s_mov_b64 exec, s[42:43]
	ds_add_u32 v77, v142 offset:34816
	s_mov_b64 exec, s[44:45]
	ds_add_u32 v78, v142 offset:34816
	s_mov_b64 exec, s[46:47]
	ds_add_u32 v79, v142 offset:34816
	s_mov_b64 exec, s[48:49]
	ds_add_u32 v80, v142 offset:34816
	s_mov_b64 exec, s[50:51]
	ds_add_u32 v81, v142 offset:34816
	s_mov_b64 exec, s[52:53]
	ds_add_u32 v82, v142 offset:34816
	s_mov_b64 exec, s[54:55]
	ds_add_u32 v83, v142 offset:34816
	s_mov_b64 exec, s[56:57]
	ds_add_u32 v84, v142 offset:34816
	s_mov_b64 exec, s[58:59]
	ds_add_u32 v85, v142 offset:34816
	s_mov_b64 exec, s[60:61]
	ds_add_u32 v86, v142 offset:34816
	s_mov_b64 exec, s[62:63]
	ds_add_u32 v87, v142 offset:34816
	s_mov_b64 exec, s[64:65]
	ds_add_u32 v88, v142 offset:34816
	s_mov_b64 exec, s[66:67]
	ds_add_u32 v89, v142 offset:34816
	s_mov_b64 exec, s[68:69]
	ds_add_u32 v90, v142 offset:34816
	s_mov_b64 exec, s[70:71]
	ds_add_u32 v91, v142 offset:34816
	s_mov_b64 exec, s[72:73]
	ds_add_u32 v92, v142 offset:34816
	s_mov_b64 exec, s[74:75]
	ds_add_u32 v93, v142 offset:34816
	s_mov_b64 exec, s[76:77]
	ds_add_u32 v94, v142 offset:34816
	s_mov_b64 exec, s[78:79]
	ds_add_u32 v95, v142 offset:34816
	s_mov_b64 exec, s[80:81]
	ds_add_u32 v96, v142 offset:34816
	s_mov_b64 exec, s[82:83]
	ds_add_u32 v97, v142 offset:34816
	s_mov_b64 exec, s[84:85]
	ds_add_u32 v98, v142 offset:34816
	s_mov_b64 exec, s[86:87]
	ds_add_u32 v99, v142 offset:34816
	s_mov_b64 exec, s[88:89]
	ds_add_u32 v100, v142 offset:34816
	s_mov_b64 exec, s[90:91]
	ds_add_u32 v101, v142 offset:34816
	s_mov_b64 exec, s[92:93]
	ds_add_u32 v102, v142 offset:34816
	s_mov_b64 exec, s[94:95]
	ds_add_u32 v103, v142 offset:34816
	s_mov_b64 exec, s[96:97]
	ds_add_u32 v104, v142 offset:34816
	s_mov_b64 exec, s[98:99]
	ds_add_u32 v105, v142 offset:34816
	s_mov_b64 exec, -1
	s_waitcnt lgkmcnt(0)
	s_barrier
	v_and_b32_e32 v67, 15, v0
	v_mul_u32_u24_e32 v67, 0x810, v67
	ds_read_b32 v68, v67 offset:34816
	s_waitcnt lgkmcnt(0)
	v_mov_b32_e32 v69, v68
	s_nop 1
	v_add_u32_dpp v69, v69, v69 row_shr:1 row_mask:0xf bank_mask:0xf bound_ctrl:1
	s_nop 1
	v_add_u32_dpp v69, v69, v69 row_shr:2 row_mask:0xf bank_mask:0xf bound_ctrl:1
	s_nop 1
	v_add_u32_dpp v69, v69, v69 row_shr:4 row_mask:0xf bank_mask:0xf bound_ctrl:1
	s_nop 1
	v_add_u32_dpp v69, v69, v69 row_shr:8 row_mask:0xf bank_mask:0xf bound_ctrl:1
	s_nop 1
	v_sub_u32_e32 v70, v69, v68
	v_lshlrev_b32_e32 v70, 2, v70
	v_readlane_b32 s8, v69, 15
	s_cmp_lg_u32 s17, 0
	s_cbranch_scc1 .Lfront_nocursor
	v_cmp_gt_u32_e32 vcc, 16, v1
	s_and_saveexec_b64 s[30:31], vcc
	ds_write_b32 v67, v70 offset:34820
	v_lshl_add_u32 v71, v1, 2, v144
	ds_write_b32 v71, v68
	s_mov_b64 exec, s[30:31]
.Lfront_nocursor:
	s_waitcnt lgkmcnt(0)
	s_barrier
	s_mov_b64 exec, s[36:37]
	ds_add_rtn_u32 v106, v74, v143 offset:34820
	s_mov_b64 exec, s[38:39]
	ds_add_rtn_u32 v107, v75, v143 offset:34820
	s_mov_b64 exec, s[40:41]
	ds_add_rtn_u32 v108, v76, v143 offset:34820
	s_mov_b64 exec, s[42:43]
	ds_add_rtn_u32 v109, v77, v143 offset:34820
	s_mov_b64 exec, s[44:45]
	ds_add_rtn_u32 v110, v78, v143 offset:34820
	s_mov_b64 exec, s[46:47]
	ds_add_rtn_u32 v111, v79, v143 offset:34820
	s_mov_b64 exec, s[48:49]
	ds_add_rtn_u32 v112, v80, v143 offset:34820
	s_mov_b64 exec, s[50:51]
	ds_add_rtn_u32 v113, v81, v143 offset:34820
	s_mov_b64 exec, s[52:53]
	ds_add_rtn_u32 v114, v82, v143 offset:34820
	s_mov_b64 exec, s[54:55]
	ds_add_rtn_u32 v115, v83, v143 offset:34820
	s_mov_b64 exec, s[56:57]
	ds_add_rtn_u32 v116, v84, v143 offset:34820
	s_mov_b64 exec, s[58:59]
	ds_add_rtn_u32 v117, v85, v143 offset:34820
	s_mov_b64 exec, s[60:61]
	ds_add_rtn_u32 v118, v86, v143 offset:34820
	s_mov_b64 exec, s[62:63]
	ds_add_rtn_u32 v119, v87, v143 offset:34820
	s_mov_b64 exec, s[64:65]
	ds_add_rtn_u32 v120, v88, v143 offset:34820
	s_mov_b64 exec, s[66:67]
	ds_add_rtn_u32 v121, v89, v143 offset:34820
	s_mov_b64 exec, s[68:69]
	ds_add_rtn_u32 v122, v90, v143 offset:34820
	s_mov_b64 exec, s[70:71]
	ds_add_rtn_u32 v123, v91, v143 offset:34820
	s_mov_b64 exec, s[72:73]
	ds_add_rtn_u32 v124, v92, v143 offset:34820
	s_mov_b64 exec, s[74:75]
	ds_add_rtn_u32 v125, v93, v143 offset:34820
	s_mov_b64 exec, s[76:77]
	ds_add_rtn_u32 v126, v94, v143 offset:34820
	s_mov_b64 exec, s[78:79]
	ds_add_rtn_u32 v127, v95, v143 offset:34820
	s_mov_b64 exec, s[80:81]
	ds_add_rtn_u32 v128, v96, v143 offset:34820
	s_mov_b64 exec, s[82:83]
	ds_add_rtn_u32 v129, v97, v143 offset:34820
	s_mov_b64 exec, s[84:85]
	ds_add_rtn_u32 v130, v98, v143 offset:34820
	s_mov_b64 exec, s[86:87]
	ds_add_rtn_u32 v131, v99, v143 offset:34820
	s_mov_b64 exec, s[88:89]
	ds_add_rtn_u32 v132, v100, v143 offset:34820
	s_mov_b64 exec, s[90:91]
	ds_add_rtn_u32 v133, v101, v143 offset:34820
	s_mov_b64 exec, s[92:93]
	ds_add_rtn_u32 v134, v102, v143 offset:34820
	s_mov_b64 exec, s[94:95]
	ds_add_rtn_u32 v135, v103, v143 offset:34820
	s_mov_b64 exec, s[96:97]
	ds_add_rtn_u32 v136, v104, v143 offset:34820
	s_mov_b64 exec, s[98:99]
	ds_add_rtn_u32 v137, v105, v143 offset:34820
	s_mov_b64 exec, -1
	v_lshlrev_b32_e32 v145, 18, v0
	v_add_u32_e32 v146, 0x0, v145
	v_or_b32_e32 v74, v146, v74
	v_add_u32_e32 v147, 0x10000, v145
	v_or_b32_e32 v75, v147, v75
	v_add_u32_e32 v146, 0x20000, v145
	v_or_b32_e32 v76, v146, v76
	v_add_u32_e32 v147, 0x30000, v145
	v_or_b32_e32 v77, v147, v77
	v_add_u32_e32 v146, 0x4000000, v145
	v_or_b32_e32 v78, v146, v78
	v_add_u32_e32 v147, 0x4010000, v145
	v_or_b32_e32 v79, v147, v79
	v_add_u32_e32 v146, 0x4020000, v145
	v_or_b32_e32 v80, v146, v80
	v_add_u32_e32 v147, 0x4030000, v145
	v_or_b32_e32 v81, v147, v81
	v_add_u32_e32 v146, 0x8000000, v145
	v_or_b32_e32 v82, v146, v82
	v_add_u32_e32 v147, 0x8010000, v145
	v_or_b32_e32 v83, v147, v83
	v_add_u32_e32 v146, 0x8020000, v145
	v_or_b32_e32 v84, v146, v84
	v_add_u32_e32 v147, 0x8030000, v145
	v_or_b32_e32 v85, v147, v85
	v_add_u32_e32 v146, 0xc000000, v145
	v_or_b32_e32 v86, v146, v86
	v_add_u32_e32 v147, 0xc010000, v145
	v_or_b32_e32 v87, v147, v87
	v_add_u32_e32 v146, 0xc020000, v145
	v_or_b32_e32 v88, v146, v88
	v_add_u32_e32 v147, 0xc030000, v145
	v_or_b32_e32 v89, v147, v89
	v_add_u32_e32 v146, 0x10000000, v145
	v_or_b32_e32 v90, v146, v90
	v_add_u32_e32 v147, 0x10010000, v145
	v_or_b32_e32 v91, v147, v91
	v_add_u32_e32 v146, 0x10020000, v145
	v_or_b32_e32 v92, v146, v92
	v_add_u32_e32 v147, 0x10030000, v145
	v_or_b32_e32 v93, v147, v93
	v_add_u32_e32 v146, 0x14000000, v145
	v_or_b32_e32 v94, v146, v94
	v_add_u32_e32 v147, 0x14010000, v145
	v_or_b32_e32 v95, v147, v95
	v_add_u32_e32 v146, 0x14020000, v145
	v_or_b32_e32 v96, v146, v96
	v_add_u32_e32 v147, 0x14030000, v145
	v_or_b32_e32 v97, v147, v97
	v_add_u32_e32 v146, 0x18000000, v145
	v_or_b32_e32 v98, v146, v98
	v_add_u32_e32 v147, 0x18010000, v145
	v_or_b32_e32 v99, v147, v99
	v_add_u32_e32 v146, 0x18020000, v145
	v_or_b32_e32 v100, v146, v100
	v_add_u32_e32 v147, 0x18030000, v145
	v_or_b32_e32 v101, v147, v101
	v_add_u32_e32 v146, 0x1c000000, v145
	v_or_b32_e32 v102, v146, v102
	v_add_u32_e32 v147, 0x1c010000, v145
	v_or_b32_e32 v103, v147, v103
	v_add_u32_e32 v146, 0x1c020000, v145
	v_or_b32_e32 v104, v146, v104
	v_add_u32_e32 v147, 0x1c030000, v145
	v_or_b32_e32 v105, v147, v105
	s_waitcnt lgkmcnt(0)
	s_mov_b64 exec, s[36:37]
	ds_write_b32 v106, v74
	s_mov_b64 exec, s[38:39]
	ds_write_b32 v107, v75
	s_mov_b64 exec, s[40:41]
	ds_write_b32 v108, v76
	s_mov_b64 exec, s[42:43]
	ds_write_b32 v109, v77
	s_mov_b64 exec, s[44:45]
	ds_write_b32 v110, v78
	s_mov_b64 exec, s[46:47]
	ds_write_b32 v111, v79
	s_mov_b64 exec, s[48:49]
	ds_write_b32 v112, v80
	s_mov_b64 exec, s[50:51]
	ds_write_b32 v113, v81
	s_mov_b64 exec, s[52:53]
	ds_write_b32 v114, v82
	s_mov_b64 exec, s[54:55]
	ds_write_b32 v115, v83
	s_mov_b64 exec, s[56:57]
	ds_write_b32 v116, v84
	s_mov_b64 exec, s[58:59]
	ds_write_b32 v117, v85
	s_mov_b64 exec, s[60:61]
	ds_write_b32 v118, v86
	s_mov_b64 exec, s[62:63]
	ds_write_b32 v119, v87
	s_mov_b64 exec, s[64:65]
	ds_write_b32 v120, v88
	s_mov_b64 exec, s[66:67]
	ds_write_b32 v121, v89
	s_mov_b64 exec, s[68:69]
	ds_write_b32 v122, v90
	s_mov_b64 exec, s[70:71]
	ds_write_b32 v123, v91
	s_mov_b64 exec, s[72:73]
	ds_write_b32 v124, v92
	s_mov_b64 exec, s[74:75]
	ds_write_b32 v125, v93
	s_mov_b64 exec, s[76:77]
	ds_write_b32 v126, v94
	s_mov_b64 exec, s[78:79]
	ds_write_b32 v127, v95
	s_mov_b64 exec, s[80:81]
	ds_write_b32 v128, v96
	s_mov_b64 exec, s[82:83]
	ds_write_b32 v129, v97
	s_mov_b64 exec, s[84:85]
	ds_write_b32 v130, v98
	s_mov_b64 exec, s[86:87]
	ds_write_b32 v131, v99
	s_mov_b64 exec, s[88:89]
	ds_write_b32 v132, v100
	s_mov_b64 exec, s[90:91]
	ds_write_b32 v133, v101
	s_mov_b64 exec, s[92:93]
	ds_write_b32 v134, v102
	s_mov_b64 exec, s[94:95]
	ds_write_b32 v135, v103
	s_mov_b64 exec, s[96:97]
	ds_write_b32 v136, v104
	s_mov_b64 exec, s[98:99]
	ds_write_b32 v137, v105
	s_mov_b64 exec, -1
	s_waitcnt lgkmcnt(0)
	s_barrier
	v_or_b32_e32 v134, s24, v138
	v_lshlrev_b32_e32 v135, 3, v1
	v_lshlrev_b32_e32 v218, 4, v1
	v_lshlrev_b32_e32 v219, 3, v1
	v_mov_b32_e32 v223, 0x11540
	v_bfrev_b32_e32 v199, 1
	v_mov_b32_e32 v198, 1
	v_and_b32_e32 v221, 15, v1
	v_mov_b32_e32 v200, 0
	v_mov_b32_e32 v201, 0
	v_mov_b32_e32 v202, 0
	v_mov_b32_e32 v203, 0
	v_mov_b32_e32 v204, 0
	v_mov_b32_e32 v205, 0
	v_mov_b32_e32 v206, 0
	v_mov_b32_e32 v207, 0
	s_mov_b32 s50, -1
	s_waitcnt vmcnt(0)
	v_mul_f32_e32 v150, v62, v62
	v_mul_f32_e32 v151, v63, v63
	v_mul_f32_e32 v152, v64, v64
	v_mul_f32_e32 v153, v65, v65
	v_fmac_f32_e32 v150, v58, v58
	v_fmac_f32_e32 v151, v59, v59
	v_fmac_f32_e32 v152, v60, v60
	v_fmac_f32_e32 v153, v61, v61
	v_fmac_f32_e32 v150, v54, v54
	v_fmac_f32_e32 v151, v55, v55
	v_fmac_f32_e32 v152, v56, v56
	v_fmac_f32_e32 v153, v57, v57
	v_fmac_f32_e32 v150, v50, v50
	v_fmac_f32_e32 v151, v51, v51
	v_fmac_f32_e32 v152, v52, v52
	v_fmac_f32_e32 v153, v53, v53
	v_fmac_f32_e32 v150, v46, v46
	v_fmac_f32_e32 v151, v47, v47
	v_fmac_f32_e32 v152, v48, v48
	v_fmac_f32_e32 v153, v49, v49
	v_fmac_f32_e32 v150, v42, v42
	v_fmac_f32_e32 v151, v43, v43
	v_fmac_f32_e32 v152, v44, v44
	v_fmac_f32_e32 v153, v45, v45
	v_fmac_f32_e32 v150, v38, v38
	v_fmac_f32_e32 v151, v39, v39
	v_fmac_f32_e32 v152, v40, v40
	v_fmac_f32_e32 v153, v41, v41
	v_fmac_f32_e32 v150, v34, v34
	v_fmac_f32_e32 v151, v35, v35
	v_fmac_f32_e32 v152, v36, v36
	v_fmac_f32_e32 v153, v37, v37
	v_fmac_f32_e32 v150, v30, v30
	v_fmac_f32_e32 v151, v31, v31
	v_fmac_f32_e32 v152, v32, v32
	v_fmac_f32_e32 v153, v33, v33
	v_fmac_f32_e32 v150, v26, v26
	v_fmac_f32_e32 v151, v27, v27
	v_fmac_f32_e32 v152, v28, v28
	v_fmac_f32_e32 v153, v29, v29
	v_fmac_f32_e32 v150, v22, v22
	v_fmac_f32_e32 v151, v23, v23
	v_fmac_f32_e32 v152, v24, v24
	v_fmac_f32_e32 v153, v25, v25
	v_fmac_f32_e32 v150, v18, v18
	v_fmac_f32_e32 v151, v19, v19
	v_fmac_f32_e32 v152, v20, v20
	v_fmac_f32_e32 v153, v21, v21
	v_fmac_f32_e32 v150, v14, v14
	v_fmac_f32_e32 v151, v15, v15
	v_fmac_f32_e32 v152, v16, v16
	v_fmac_f32_e32 v153, v17, v17
	v_fmac_f32_e32 v150, v10, v10
	v_fmac_f32_e32 v151, v11, v11
	v_fmac_f32_e32 v152, v12, v12
	v_fmac_f32_e32 v153, v13, v13
	v_fmac_f32_e32 v150, v6, v6
	v_fmac_f32_e32 v151, v7, v7
	v_fmac_f32_e32 v152, v8, v8
	v_fmac_f32_e32 v153, v9, v9
	v_fmac_f32_e32 v150, v2, v2
	v_fmac_f32_e32 v151, v3, v3
	v_fmac_f32_e32 v152, v4, v4
	v_fmac_f32_e32 v153, v5, v5
	v_add_f32_e32 v150, v150, v151
	v_add_f32_e32 v152, v152, v153
	v_add_f32_e32 v150, v150, v152
	v_mbcnt_lo_u32_b32 v151, -1, 0
	v_mbcnt_hi_u32_b32 v151, -1, v151
	v_xor_b32_e32 v152, 16, v151
	v_lshlrev_b32_e32 v152, 2, v152
	ds_bpermute_b32 v152, v152, v150
	v_xor_b32_e32 v153, 32, v151
	v_lshlrev_b32_e32 v153, 2, v153
	s_waitcnt lgkmcnt(0)
	v_add_f32_e32 v150, v150, v152
	ds_bpermute_b32 v153, v153, v150
	v_add_u32_e32 v152, s24, v1
	v_lshlrev_b32_e32 v152, 2, v152
	v_add_u32_e32 v152, 0x11300, v152
	v_cmp_gt_u32_e32 vcc, 16, v1
	s_and_saveexec_b64 s[30:31], vcc
	s_waitcnt lgkmcnt(0)
	v_add_f32_e32 v150, v150, v153
	ds_write_b32 v152, v150
	s_mov_b64 exec, s[30:31]
	s_branch .Lg0_start

.Lg_alldone:
.Lg_nocopy:
	v_cmp_eq_u32_e64 s[2:3], 0, v1
